# baseline (speedup 1.0000x reference)
_Z10snn_kernel6Params:
	s_load_dwordx16 s[44:59], s[0:1], 0x0
	s_load_dwordx8 s[60:67], s[0:1], 0x40
	s_load_dwordx2 s[72:73], s[0:1], 0x60
	v_and_b32_e32 v98, 0x3ff, v0
	s_lshr_b32 s33, s2, 3
	s_and_b32 s75, s2, 7
	s_lshl_b32 s3, s33, 4
	v_and_b32_e32 v73, 63, v98
	v_lshrrev_b32_e32 v72, 4, v98
	v_and_b32_e32 v70, 15, v98
	v_and_b32_e32 v75, 15, v72
	v_lshlrev_b32_e32 v74, 4, v98
	v_and_b32_e32 v63, 31, v98
	v_readfirstlane_b32 s76, v98
	s_mul_i32 s74, s75, 48
	s_lshl_b32 s79, s75, 5
	s_add_i32 s78, s79, s33
	s_mov_b32 s68, 0
	s_movk_i32 s6, 0xff
	v_cmp_lt_u32_e64 s[42:43], s6, v98
	v_cmp_eq_u32_e64 s[4:5], 0, v73
	v_cmp_eq_u32_e64 s[8:9], 0, v63
	v_mov_b32_e32 v34, 0
	s_lshr_b32 s10, s76, 6
	s_and_b32 s91, s33, 15
	s_lshl_b32 s91, s91, 1
	s_lshr_b32 s90, s33, 4
	s_or_b32 s91, s91, s90
	s_sub_i32 s91, s91, s33
	s_lshl_b32 s90, s91, 2
	s_waitcnt lgkmcnt(0)
	v_or_b32_e32 v252, s3, v75
	s_lshl_b32 s82, s75, 9
	v_add_u32_e32 v253, s82, v252
	v_lshlrev_b32_e32 v252, 2, v252
	v_lshlrev_b32_e32 v253, 2, v253
	v_and_b32_e32 v161, 0xff, v98
	v_lshlrev_b32_e32 v161, 2, v161
	global_load_dword v252, v252, s[56:57]
	global_load_dword v253, v253, s[58:59]
	global_load_dword v162, v161, s[50:51] offset:1024
	global_load_dword v161, v161, s[50:51]
	v_add_u32_e32 v0, s74, v72
	v_lshlrev_b32_e32 v0, 9, v0
	v_add3_u32 v0, v0, s3, v70
	v_lshlrev_b32_e32 v0, 2, v0
	global_load_dword v67, v0, s[44:45]
	v_add_u32_e32 v1, 0x10000, v0
	s_cmp_gt_u32 s10, 3
	s_cbranch_scc1 .Lco_noin1
	global_load_dword v68, v1, s[44:45]

.Lk_276:
	s_or_b64 exec, exec, s[10:11]
	v_readfirstlane_b32 s18, v2
	s_mov_b32 s10, 0x3d064869
	s_and_b32 s12, s18, 0xffff0000
	v_cvt_f32_f64_e32 v4, v[0:1]
	s_mov_b32 s11, 0x3d47c3ae
	s_cmp_lg_u32 s12, 0x30000
	s_cbranch_scc1 .Lk_282
	v_cmp_gt_u32_e32 vcc, 32, v73
	s_and_saveexec_b64 s[12:13], vcc
	s_cbranch_execz .Lk_279
	s_add_i32 s18, s18, s21
	s_and_b32 s18, s18, 0xffff
	s_lshl_b32 s19, s68, 16
	v_or_b32_e32 v2, s79, v73
	s_or_b32 s18, s18, s19
	v_lshl_add_u32 v2, v2, 5, s33
	v_mov_b32_e32 v3, 0
	s_bitset1_b32 s18, 20
	v_lshlrev_b32_e32 v6, 2, v2
	v_lshlrev_b64 v[2:3], 7, v[2:3]
	v_mov_b32_e32 v7, s18
	v_lshl_add_u64 v[2:3], s[66:67], 0, v[2:3]
	v_add_u32_e32 v6, s90, v6
	global_store_dword v6, v7, s[14:15] sc0
	global_store_dword v[2:3], v7, off sc1

.Lk_283:
	s_or_b64 exec, exec, s[0:1]
	v_lshrrev_b32_e32 v4, 4, v160
	s_lshl_b32 s0, s78, 5
	v_or_b32_e32 v165, s0, v4
	v_mov_b32_e32 v4, 0x24400
	s_add_i32 s69, s33, 33
	v_lshl_or_b32 v169, v72, 2, v4
	v_mul_u32_u24_e32 v4, 10, v160
	s_cmp_gt_i32 s77, 8
	s_cselect_b64 s[18:19], -1, 0
	s_cmp_gt_i32 s77, 10
	v_lshlrev_b32_e32 v12, 2, v4
	v_mov_b32_e32 v13, 0
	v_or_b32_e32 v164, 0x100, v160
	v_cvt_f64_f32_e32 v[10:11], v5
	v_mov_b32_e32 v5, 0x10000
	s_cselect_b64 s[20:21], -1, 0
	s_cmp_gt_i32 s77, 12
	v_lshl_add_u64 v[14:15], s[48:49], 0, v[12:13]
	v_lshlrev_b32_e32 v4, 9, v70
	v_lshlrev_b32_e32 v12, 2, v70
	v_lshl_or_b32 v67, v160, 2, v5
	v_lshl_or_b32 v69, v164, 2, v5
	s_cselect_b64 s[22:23], -1, 0
	v_add3_u32 v172, v4, s3, v75
	v_lshl_add_u64 v[4:5], s[60:61], 0, v[12:13]
	s_add_i32 s24, s24, s3
	v_lshl_add_u64 v[40:41], v[4:5], 0, 64
	v_add_u32_e32 v4, s24, v75
	v_mov_b32_e32 v5, v13
	v_lshlrev_b64 v[4:5], 11, v[4:5]
	v_cmp_gt_f32_e32 vcc, 0, v161
	v_or_b32_e32 v4, v4, v12
	v_lshrrev_b32_e32 v6, 4, v164
	v_cndmask_b32_e64 v167, 0, 1.0, vcc
	v_cmp_gt_f32_e32 vcc, 0, v162
	s_mov_b64 s[10:11], 0x2800
	s_lshl_b32 s70, s68, 16
	v_lshl_add_u64 v[4:5], s[72:73], 0, v[4:5]
	v_mov_b32_e32 v12, v13
	s_mov_b32 s26, 0x3f7d73e7
	s_mov_b32 s28, 0xa37fcc69
	s_mov_b32 s34, 0x3f779b79
	s_mov_b32 s36, 0x3d064869
	v_or_b32_e32 v166, s0, v6
	v_cndmask_b32_e64 v168, 0, 1.0, vcc
	v_cmp_gt_u32_e64 s[0:1], 32, v73
	v_lshl_add_u32 v170, v73, 5, s33
	v_lshl_add_u64 v[34:35], v[14:15], 0, s[10:11]
	s_bitset1_b32 s70, 21
	v_lshlrev_b32_e32 v171, 3, v70
	v_lshl_add_u64 v[42:43], v[4:5], 0, 64
	s_mov_b64 s[38:39], 0
	v_mov_b64_e32 v[44:45], 0
	s_mov_b64 s[24:25], 0
	s_mov_b32 s27, 0x3d8414e8
	s_mov_b32 s29, 0x3fee7078
	s_mov_b32 s3, 0xf000
	s_mov_b64 s[30:31], 0x80
	s_mov_b32 s35, 0x3f7383c5
	s_mov_b32 s37, 0x3d47c3ae
	s_mov_b32 s71, 0xffff
	v_mov_b32_e32 v47, 0x3f6f7d63
	v_bfrev_b32_e32 v173, 1
	v_mov_b32_e32 v174, 0x2f0
	v_mov_b32_e32 v175, 0x26c10
	s_mov_b64 s[40:41], 0
	s_mov_b64 s[44:45], 0
	v_mov_b32_e32 v176, 0
	v_mov_b64_e32 v[36:37], 0
	v_mov_b64_e32 v[6:7], 0
	v_mov_b64_e32 v[48:49], 0
	v_mov_b64_e32 v[38:39], 0
	v_mov_b64_e32 v[4:5], 0
	v_mov_b32_e32 v177, 0
	v_mov_b64_e32 v[50:51], v[12:13]
	v_mov_b64_e32 v[56:57], v[12:13]
	v_mov_b64_e32 v[52:53], v[12:13]
	v_mov_b64_e32 v[58:59], v[12:13]
	v_mov_b32_e32 v54, v13
	v_mov_b32_e32 v55, v13
	v_mul_f32_e32 v218, v9, v18
	v_mul_f32_e32 v219, v131, v19
	v_mul_f32_e32 v220, v134, v20
	v_mul_f32_e32 v221, v137, v21
	v_mul_f32_e32 v222, v140, v22
	v_mul_f32_e32 v223, v143, v23
	v_mul_f32_e32 v224, v146, v24
	v_mul_f32_e32 v225, v150, v25
	v_mul_f32_e32 v226, v121, v26
	v_mul_f32_e32 v227, v122, v27
	v_mov_b32_e32 v250, 0
	v_add_u16_e32 v208, v250, v159
	v_add_u16_e32 v209, v250, v158
	v_add_u16_e32 v210, v250, v157
	v_add_u16_e32 v211, v250, v156
	v_add_u16_e32 v212, v250, v155
	v_add_u16_e32 v213, v250, v154
	v_add_u16_e32 v214, v250, v153
	v_add_u16_e32 v215, v250, v149
	v_add_u16_e32 v216, v250, v128
	v_add_u16_e32 v217, v250, v127
	s_mov_b64 s[86:87], 0
	s_and_saveexec_b64 s[82:83], s[42:43]
	v_and_b32_e32 v208, 15, v165
	v_add_lshl_u32 v208, v208, v165, 2
	v_add_u32_e32 v208, 0x400000, v208
	v_add_u32_e32 v210, 4, v208
	v_mov_b32_e32 v209, 0x8000
	v_mov_b32_e32 v211, 0x8000
	s_mov_b64 exec, s[82:83]
	s_branch .Lk_288

.Lmy_no89:
	s_waitcnt lgkmcnt(0)
	v_readfirstlane_b32 s60, v12
	s_and_b32 s10, s60, 0xffff0000
	s_cmp_lg_u32 s10, 0x30000
	s_cbranch_scc1 .Lk_285
	s_and_saveexec_b64 s[10:11], s[0:1]
	s_cbranch_execz .Lk_324
	v_lshl_add_u32 v12, v177, 20, s70
	v_add_u32_e32 v248, s60, v248
	v_and_or_b32 v60, v248, s71, v12
	v_lshlrev_b32_e32 v12, 3, v178
	v_and_or_b32 v12, v12, 24, s75
	v_lshl_add_u32 v12, v12, 10, v170
	v_add_u32_e32 v250, s91, v12
	v_mov_b32_e32 v251, 0
	v_lshl_add_u64 v[248:249], v[250:251], 2, s[14:15]
	global_store_dword v[248:249], v60, off sc0
	v_lshlrev_b64 v[248:249], 7, v[12:13]
	v_lshl_add_u64 v[248:249], s[66:67], 0, v[248:249]
	global_store_dword v[248:249], v60, off sc1

.Lmy_rx:
	v_and_b32_e32 v212, 3, v177
	v_mad_u32_u24 v213, v212, v209, v208
	v_mad_u32_u24 v214, v212, v211, v210
	s_and_b64 s[82:83], s[38:39], s[40:41]
	s_cmp_eq_u64 s[82:83], exec
	s_cbranch_scc1 .Lmy_rx_one
	global_load_dword v182, v213, s[66:67] sc1
	global_load_dword v183, v214, s[66:67] sc1
	s_branch .Lmy_rx_ld
.Lmy_rx_one:
	global_load_dwordx2 v[182:183], v213, s[66:67] sc1
.Lmy_rx_ld:
	v_cmp_eq_u32_e64 s[10:11], 0, v177
	v_cmp_ne_u32_e32 vcc, 0, v177
	s_and_saveexec_b64 s[12:13], vcc
	s_cbranch_execz .Lk_291
	v_mul_f32_e32 v60, v161, v59
	v_fma_f32 v46, v167, v52, 1.0
	v_mov_b32_e32 v61, v53
	v_pk_mul_f32 v[52:53], v[60:61], v[46:47]
	v_add_u32_e32 v12, -1, v177
	v_pk_fma_f32 v[52:53], v[58:59], s[26:27], v[52:53]
	v_cvt_f64_f32_e32 v[58:59], v59
	v_fmac_f64_e32 v[58:59], s[28:29], v[44:45]
	v_cvt_f64_f32_e32 v[44:45], v57
	v_mul_f32_e32 v62, v162, v57
	v_fma_f32 v50, v168, v50, 1.0
	v_mov_b32_e32 v63, v51
	v_mov_b32_e32 v51, v47
	v_fmac_f64_e32 v[44:45], s[28:29], v[48:49]
	v_cmp_eq_u32_e32 vcc, s33, v12
	v_pk_mul_f32 v[50:51], v[62:63], v[50:51]
	v_mov_b64_e32 v[48:49], v[44:45]
	v_cndmask_b32_e32 v39, v39, v45, vcc
	v_cndmask_b32_e32 v38, v38, v44, vcc
	v_cndmask_b32_e32 v37, v37, v59, vcc
	v_cndmask_b32_e32 v36, v36, v58, vcc
	v_cmp_eq_u32_e32 vcc, s69, v177
	v_pk_fma_f32 v[50:51], v[56:57], s[26:27], v[50:51]
	s_nop 0
	v_cndmask_b32_e32 v5, v5, v45, vcc
	v_cndmask_b32_e32 v4, v4, v44, vcc
	v_cndmask_b32_e32 v7, v7, v59, vcc
	v_cndmask_b32_e32 v6, v6, v58, vcc
	v_mov_b64_e32 v[44:45], v[58:59]

.Lk_303:
	s_or_b64 exec, exec, s[48:49]
	v_lshrrev_b32_e32 v57, v70, v64
	v_lshrrev_b32_e32 v65, v70, v46
	v_bfe_i32 v60, v57, 0, 1
	v_bfe_i32 v62, v65, 0, 1
	v_and_b32_e32 v60, v60, v216
	v_and_b32_e32 v62, v62, v217
	ds_write2_b32 v250, v60, v53 offset1:1
	ds_write2_b32 v251, v62, v51 offset1:1
	v_and_b32_e32 v59, 1, v57
	v_and_b32_e32 v57, 1, v65
	v_cvt_f32_ubyte0_e32 v59, v59
	v_cvt_f32_ubyte0_e32 v57, v57
	v_mov_b32_e32 v56, v50
	v_mov_b32_e32 v58, v52
	s_cmp_eq_u64 s[10:11], 0
	s_cbranch_scc1 .Lmy_rx_nt0
	v_bfe_u32 v60, v46, 16, 4
	v_bfe_u32 v61, v64, 16, 4
	v_cmp_eq_u32_e64 s[48:49], s68, v60
	v_cmp_eq_u32_e64 s[50:51], s68, v61
	v_and_b32_e32 v60, 15, v165
	v_add_lshl_u32 v60, v60, v165, 2
	v_add_u32_e32 v60, 0x400000, v60
	v_add_u32_e32 v61, 4, v60
	v_lshlrev_b32_e32 v62, 7, v165
	v_lshlrev_b32_e32 v63, 7, v166
	v_cndmask_b32_e64 v208, v62, v60, s[50:51]
	v_cndmask_b32_e64 v210, v63, v61, s[48:49]
	v_mov_b32_e32 v60, 0x8000
	v_mov_b32_e32 v62, 0x100000
	v_cndmask_b32_e64 v209, v62, v60, s[50:51]
	v_cndmask_b32_e64 v211, v62, v60, s[48:49]
	s_branch .Lmy_rx_end
